# MoE epilogue waits counted after stores; inproj: first K-iteration peeled, preheader drain skipped after an epilogue, counted wait after stores
# baseline (speedup 1.0000x reference)
.LBB0_131:
	s_add_u32 s4, s0, 0xc100000
	s_addc_u32 s5, s1, 0
	s_lshl_b32 s9, s9, 5
	s_and_b32 s9, s9, 0x60
	s_add_i32 m0, s15, 0x18000
	v_lshl_add_u64 v[8:9], v[8:9], 0, s[46:47]
	s_lshl_b32 s12, s8, 13
	s_lshl_b32 s13, s9, 7
	s_waitcnt vmcnt(2)
	s_barrier
	global_load_lds_dwordx4 v[8:9], off
	v_lshl_add_u64 v[6:7], v[6:7], 0, s[46:47]
	s_add_i32 m0, s15, 0x1a000
	s_add_i32 s38, s15, 0x8000
	s_add_i32 s39, s15, 0xa000
	global_load_lds_dwordx4 v[6:7], off
	v_lshl_add_u64 v[2:3], v[2:3], 0, s[46:47]
	s_mov_b32 m0, s38
	s_add_u32 s10, s18, 0x40080
	global_load_lds_dwordx4 v[2:3], off
	v_lshl_add_u64 v[2:3], v[4:5], 0, s[46:47]
	s_mov_b32 m0, s39
	s_addc_u32 s11, s19, 0
	global_load_lds_dwordx4 v[2:3], off
	s_add_i32 m0, s15, 0x1c000
	v_lshl_add_u64 v[2:3], s[10:11], 0, v[0:1]
	global_load_lds_dwordx4 v[2:3], off
	v_lshl_add_u64 v[2:3], s[10:11], 0, v[134:135]
	s_add_i32 m0, s15, 0x1e000
	s_cmpk_lt_u32 s7, 0x100
	global_load_lds_dwordx4 v[2:3], off
	v_lshrrev_b32_e32 v3, 1, v10
	v_and_b32_e32 v4, 24, v3
	v_and_b32_e32 v2, 15, v10
	v_lshlrev_b32_e32 v3, 1, v4
	s_sext_i32_i8 s50, s6
	v_lshl_or_b32 v162, s8, 6, v2
	v_lshl_or_b32 v2, v2, 6, v3
	v_lshlrev_b32_e32 v3, 2, v10
	s_cselect_b64 s[6:7], -1, 0
	s_ashr_i32 s42, s26, 31
	s_lshl_b32 s8, s9, 2
	v_and_b32_e32 v3, 32, v3
	s_add_u32 s0, s0, s8
	v_bitop3_b32 v5, v2, s12, v3 bitop3:0xde
	v_bitop3_b32 v163, s13, v2, v3 bitop3:0xf6
	s_addc_u32 s1, s1, 0
	v_lshlrev_b32_e32 v2, 2, v4
	v_mov_b32_e32 v3, v1
	v_lshl_add_u64 v[2:3], s[0:1], 0, v[2:3]
	s_mov_b64 s[0:1], 0x13100000
	v_lshl_add_u64 v[140:141], v[2:3], 0, s[0:1]
	v_lshlrev_b32_e32 v2, 14, v11
	v_and_b32_e32 v2, 0xffff8000, v2
	v_lshl_add_u32 v2, v12, 11, v2
	v_and_b32_e32 v3, 1, v11
	v_lshl_or_b32 v2, v3, 6, v2
	v_lshl_add_u32 v142, v13, 1, v2
	v_lshlrev_b32_e32 v2, 14, v15
	v_and_b32_e32 v2, 0xffff8000, v2
	s_waitcnt vmcnt(6)
	v_lshl_add_u32 v2, v14, 11, v2
	v_and_b32_e32 v3, 1, v15
	v_lshl_or_b32 v2, v3, 6, v2
	v_or_b32_e32 v164, s9, v4
	v_mov_b32_e32 v143, v1
	v_lshl_add_u32 v144, v16, 1, v2
	v_mov_b32_e32 v145, v1
	s_mov_b32 s43, 0
	v_add_u32_e32 v165, 0, v5
	s_barrier
	s_mov_b32 s32, 0
	s_branch .LBB0_134

.LBB0_136:
	s_ashr_i32 s11, s10, 31
	s_lshl_b64 s[12:13], s[10:11], 19
	s_add_u32 s12, s27, s12
	s_addc_u32 s13, s28, s13
	s_and_b64 s[16:17], s[0:1], exec
	s_cselect_b32 s11, s13, s21
	s_cselect_b32 s51, s12, s20
	s_ashr_i32 s9, s8, 31
	s_lshl_b64 s[16:17], s[8:9], 19
	s_add_u32 s16, s29, s16
	s_addc_u32 s17, s30, s17
	s_and_b64 s[22:23], s[0:1], exec
	s_cselect_b32 s9, s17, s19
	s_cselect_b32 s52, s16, s18
	s_add_u32 s53, s18, 0x100
	s_addc_u32 s54, s19, 0
	s_add_u32 s18, s20, 0x40080
	s_addc_u32 s19, s21, 0
	s_mov_b32 s55, -2
	s_cmp_lg_u32 s32, 0
	s_cbranch_scc1 .Lip_pre
	s_waitcnt vmcnt(0)
.Lip_pre:
	s_add_u32 s20, s18, 0xfffc0080
	s_addc_u32 s21, s19, -1
	s_add_i32 s33, 0, 0x10000
	s_cmp_eq_u32 s55, 12
	s_cselect_b32 s23, s11, s21
	s_cselect_b32 s22, s51, s20
	s_cselect_b32 s21, s9, s54
	s_cselect_b32 s20, s52, s53
	s_add_i32 s44, 0, 0x14000
	v_add_u32_e32 v158, s33, v163
	v_add_u32_e32 v178, s44, v163
	ds_read_b128 v[146:149], v158
	ds_read_b128 v[150:153], v158 offset:1024
	ds_read_b128 v[154:157], v158 offset:2048
	ds_read_b128 v[158:161], v158 offset:3072
	ds_read_b128 v[166:169], v178
	ds_read_b128 v[170:173], v178 offset:1024
	ds_read_b128 v[174:177], v178 offset:2048
	ds_read_b128 v[178:181], v178 offset:3072
	v_lshl_add_u64 v[182:183], s[18:19], 0, v[144:145]
	s_add_i32 m0, s15, 0xc000
	ds_read_b128 v[186:189], v165
	ds_read_b128 v[190:193], v165 offset:1024
	ds_read_b128 v[194:197], v165 offset:2048
	ds_read_b128 v[198:201], v165 offset:3072
	ds_read_b128 v[224:227], v165 offset:4096
	ds_read_b128 v[228:231], v165 offset:5120
	ds_read_b128 v[232:235], v165 offset:6144
	ds_read_b128 v[236:239], v165 offset:7168
	global_load_lds_dwordx4 v[182:183], off
	v_lshl_add_u64 v[182:183], s[18:19], 0, v[142:143]
	s_add_i32 m0, s15, 0xe000
	s_nop 0
	global_load_lds_dwordx4 v[182:183], off
	s_cmp_lg_u32 s32, 0
	s_cbranch_scc1 .Lip_w1
	s_waitcnt vmcnt(8)
.Lip_w1:
	s_waitcnt lgkmcnt(0)
	s_barrier
	s_setprio 1
	s_waitcnt lgkmcnt(0)
	v_mfma_f32_16x16x32_bf16 v[130:133], v[146:149], v[186:189], 0
	v_mfma_f32_16x16x32_bf16 v[126:129], v[154:157], v[186:189], 0
	v_mfma_f32_16x16x32_bf16 v[122:125], v[146:149], v[194:197], 0
	v_mfma_f32_16x16x32_bf16 v[118:121], v[154:157], v[194:197], 0
	v_mfma_f32_16x16x32_bf16 v[114:117], v[146:149], v[224:227], 0
	v_mfma_f32_16x16x32_bf16 v[110:113], v[154:157], v[224:227], 0
	v_mfma_f32_16x16x32_bf16 v[98:101], v[146:149], v[232:235], 0
	v_mfma_f32_16x16x32_bf16 v[94:97], v[154:157], v[232:235], 0
	v_mfma_f32_16x16x32_bf16 v[130:133], v[150:153], v[190:193], v[130:133]
	v_mfma_f32_16x16x32_bf16 v[126:129], v[158:161], v[190:193], v[126:129]
	v_mfma_f32_16x16x32_bf16 v[122:125], v[150:153], v[198:201], v[122:125]
	v_mfma_f32_16x16x32_bf16 v[118:121], v[158:161], v[198:201], v[118:121]
	v_mfma_f32_16x16x32_bf16 v[114:117], v[150:153], v[228:231], v[114:117]
	v_mfma_f32_16x16x32_bf16 v[110:113], v[158:161], v[228:231], v[110:113]
	v_mfma_f32_16x16x32_bf16 v[98:101], v[150:153], v[236:239], v[98:101]
	v_mfma_f32_16x16x32_bf16 v[94:97], v[158:161], v[236:239], v[94:97]
	s_setprio 0
	s_setprio 1
	v_mfma_f32_16x16x32_bf16 v[106:109], v[166:169], v[186:189], 0
	v_mfma_f32_16x16x32_bf16 v[102:105], v[174:177], v[186:189], 0
	v_mfma_f32_16x16x32_bf16 v[90:93], v[166:169], v[194:197], 0
	v_mfma_f32_16x16x32_bf16 v[86:89], v[174:177], v[194:197], 0
	v_mfma_f32_16x16x32_bf16 v[82:85], v[166:169], v[224:227], 0
	v_mfma_f32_16x16x32_bf16 v[78:81], v[174:177], v[224:227], 0
	v_mfma_f32_16x16x32_bf16 v[74:77], v[166:169], v[232:235], 0
	v_mfma_f32_16x16x32_bf16 v[70:73], v[174:177], v[232:235], 0
	v_mfma_f32_16x16x32_bf16 v[106:109], v[170:173], v[190:193], v[106:109]
	v_mfma_f32_16x16x32_bf16 v[102:105], v[178:181], v[190:193], v[102:105]
	v_mfma_f32_16x16x32_bf16 v[90:93], v[170:173], v[198:201], v[90:93]
	v_mfma_f32_16x16x32_bf16 v[86:89], v[178:181], v[198:201], v[86:89]
	v_mfma_f32_16x16x32_bf16 v[82:85], v[170:173], v[228:231], v[82:85]
	v_mfma_f32_16x16x32_bf16 v[78:81], v[178:181], v[228:231], v[78:81]
	v_mfma_f32_16x16x32_bf16 v[74:77], v[170:173], v[236:239], v[74:77]
	v_mfma_f32_16x16x32_bf16 v[70:73], v[178:181], v[236:239], v[70:73]
	s_setprio 0
	s_barrier
	s_add_i32 s33, s33, s31
	v_lshl_add_u64 v[182:183], s[20:21], 0, v[0:1]
	s_mov_b32 m0, s33
	ds_read_b128 v[186:189], v165 offset:16384
	ds_read_b128 v[190:193], v165 offset:17408
	ds_read_b128 v[194:197], v165 offset:18432
	ds_read_b128 v[198:201], v165 offset:19456
	ds_read_b128 v[224:227], v165 offset:20480
	ds_read_b128 v[228:231], v165 offset:21504
	ds_read_b128 v[232:235], v165 offset:22528
	ds_read_b128 v[236:239], v165 offset:23552
	global_load_lds_dwordx4 v[182:183], off
	s_add_i32 m0, s33, 0x2000
	s_add_u32 s40, s20, 0x40000
	v_lshl_add_u64 v[184:185], s[20:21], 0, v[134:135]
	s_addc_u32 s41, s21, 0
	s_add_i32 s33, s44, s31
	global_load_lds_dwordx4 v[184:185], off
	v_lshl_add_u64 v[202:203], s[40:41], 0, v[0:1]
	s_mov_b32 m0, s33
	v_lshl_add_u64 v[210:211], s[22:23], 0, v[136:137]
	global_load_lds_dwordx4 v[202:203], off
	v_lshl_add_u64 v[202:203], s[40:41], 0, v[134:135]
	s_add_i32 m0, s33, 0x2000
	s_nop 0
	global_load_lds_dwordx4 v[202:203], off
	v_lshl_add_u64 v[202:203], s[22:23], 0, v[138:139]
	s_mov_b32 m0, s15
	s_nop 0
	global_load_lds_dwordx4 v[202:203], off
	s_mov_b32 m0, s35
	s_nop 0
	global_load_lds_dwordx4 v[210:211], off
	s_cmp_lg_u32 s32, 0
	s_cbranch_scc1 .Lip_w2
	s_waitcnt vmcnt(8)
.Lip_w2:
	s_waitcnt lgkmcnt(0)
	s_barrier
	s_setprio 1
	s_waitcnt lgkmcnt(0)
	v_mfma_f32_16x16x32_bf16 v[66:69], v[146:149], v[186:189], 0
	v_mfma_f32_16x16x32_bf16 v[62:65], v[154:157], v[186:189], 0
	v_mfma_f32_16x16x32_bf16 v[58:61], v[146:149], v[194:197], 0
	v_mfma_f32_16x16x32_bf16 v[54:57], v[154:157], v[194:197], 0
	v_mfma_f32_16x16x32_bf16 v[50:53], v[146:149], v[224:227], 0
	v_mfma_f32_16x16x32_bf16 v[46:49], v[154:157], v[224:227], 0
	v_mfma_f32_16x16x32_bf16 v[30:33], v[146:149], v[232:235], 0
	v_mfma_f32_16x16x32_bf16 v[26:29], v[154:157], v[232:235], 0
	v_mfma_f32_16x16x32_bf16 v[66:69], v[150:153], v[190:193], v[66:69]
	v_mfma_f32_16x16x32_bf16 v[62:65], v[158:161], v[190:193], v[62:65]
	v_mfma_f32_16x16x32_bf16 v[58:61], v[150:153], v[198:201], v[58:61]
	v_mfma_f32_16x16x32_bf16 v[54:57], v[158:161], v[198:201], v[54:57]
	v_mfma_f32_16x16x32_bf16 v[50:53], v[150:153], v[228:231], v[50:53]
	v_mfma_f32_16x16x32_bf16 v[46:49], v[158:161], v[228:231], v[46:49]
	v_mfma_f32_16x16x32_bf16 v[30:33], v[150:153], v[236:239], v[30:33]
	v_mfma_f32_16x16x32_bf16 v[26:29], v[158:161], v[236:239], v[26:29]
	s_setprio 0
	s_setprio 1
	v_mfma_f32_16x16x32_bf16 v[42:45], v[166:169], v[186:189], 0
	v_mfma_f32_16x16x32_bf16 v[38:41], v[174:177], v[186:189], 0
	v_mfma_f32_16x16x32_bf16 v[22:25], v[166:169], v[194:197], 0
	v_mfma_f32_16x16x32_bf16 v[18:21], v[174:177], v[194:197], 0
	v_mfma_f32_16x16x32_bf16 v[14:17], v[166:169], v[224:227], 0
	v_mfma_f32_16x16x32_bf16 v[10:13], v[174:177], v[224:227], 0
	v_mfma_f32_16x16x32_bf16 v[6:9], v[166:169], v[232:235], 0
	v_mfma_f32_16x16x32_bf16 v[2:5], v[174:177], v[232:235], 0
	v_mfma_f32_16x16x32_bf16 v[42:45], v[170:173], v[190:193], v[42:45]
	v_mfma_f32_16x16x32_bf16 v[38:41], v[178:181], v[190:193], v[38:41]
	v_mfma_f32_16x16x32_bf16 v[22:25], v[170:173], v[198:201], v[22:25]
	v_mfma_f32_16x16x32_bf16 v[18:21], v[178:181], v[198:201], v[18:21]
	v_mfma_f32_16x16x32_bf16 v[14:17], v[170:173], v[228:231], v[14:17]
	v_mfma_f32_16x16x32_bf16 v[10:13], v[178:181], v[228:231], v[10:13]
	v_mfma_f32_16x16x32_bf16 v[6:9], v[170:173], v[236:239], v[6:9]
	v_mfma_f32_16x16x32_bf16 v[2:5], v[178:181], v[236:239], v[2:5]
	s_setprio 0
	s_barrier
	s_add_i32 s33, 0, 0x18000
	s_add_i32 s40, 0, 0x1c000
	v_add_u32_e32 v158, s33, v163
	v_add_u32_e32 v178, s40, v163
	ds_read_b128 v[146:149], v158
	ds_read_b128 v[150:153], v158 offset:1024
	ds_read_b128 v[154:157], v158 offset:2048
	ds_read_b128 v[158:161], v158 offset:3072
	ds_read_b128 v[166:169], v178
	ds_read_b128 v[170:173], v178 offset:1024
	ds_read_b128 v[174:177], v178 offset:2048
	ds_read_b128 v[178:181], v178 offset:3072
	s_add_u32 s22, s22, 0x40000
	s_addc_u32 s23, s23, 0
	s_mov_b32 m0, s36
	v_lshl_add_u64 v[218:219], s[22:23], 0, v[138:139]
	ds_read_b128 v[186:189], v165 offset:32768
	ds_read_b128 v[190:193], v165 offset:33792
	ds_read_b128 v[194:197], v165 offset:34816
	ds_read_b128 v[198:201], v165 offset:35840
	ds_read_b128 v[224:227], v165 offset:36864
	ds_read_b128 v[228:231], v165 offset:37888
	ds_read_b128 v[232:235], v165 offset:38912
	ds_read_b128 v[236:239], v165 offset:39936
	global_load_lds_dwordx4 v[218:219], off
	v_lshl_add_u64 v[218:219], s[22:23], 0, v[136:137]
	s_mov_b32 m0, s37
	s_nop 0
	global_load_lds_dwordx4 v[218:219], off
	s_waitcnt vmcnt(8)
	s_waitcnt lgkmcnt(0)
	s_barrier
	s_setprio 1
	s_waitcnt lgkmcnt(0)
	v_mfma_f32_16x16x32_bf16 v[130:133], v[146:149], v[186:189], v[130:133]
	v_mfma_f32_16x16x32_bf16 v[126:129], v[154:157], v[186:189], v[126:129]
	v_mfma_f32_16x16x32_bf16 v[122:125], v[146:149], v[194:197], v[122:125]
	v_mfma_f32_16x16x32_bf16 v[118:121], v[154:157], v[194:197], v[118:121]
	v_mfma_f32_16x16x32_bf16 v[114:117], v[146:149], v[224:227], v[114:117]
	v_mfma_f32_16x16x32_bf16 v[110:113], v[154:157], v[224:227], v[110:113]
	v_mfma_f32_16x16x32_bf16 v[98:101], v[146:149], v[232:235], v[98:101]
	v_mfma_f32_16x16x32_bf16 v[94:97], v[154:157], v[232:235], v[94:97]
	v_mfma_f32_16x16x32_bf16 v[130:133], v[150:153], v[190:193], v[130:133]
	v_mfma_f32_16x16x32_bf16 v[126:129], v[158:161], v[190:193], v[126:129]
	v_mfma_f32_16x16x32_bf16 v[122:125], v[150:153], v[198:201], v[122:125]
	v_mfma_f32_16x16x32_bf16 v[118:121], v[158:161], v[198:201], v[118:121]
	v_mfma_f32_16x16x32_bf16 v[114:117], v[150:153], v[228:231], v[114:117]
	v_mfma_f32_16x16x32_bf16 v[110:113], v[158:161], v[228:231], v[110:113]
	v_mfma_f32_16x16x32_bf16 v[98:101], v[150:153], v[236:239], v[98:101]
	v_mfma_f32_16x16x32_bf16 v[94:97], v[158:161], v[236:239], v[94:97]
	s_setprio 0
	s_setprio 1
	v_mfma_f32_16x16x32_bf16 v[106:109], v[166:169], v[186:189], v[106:109]
	v_mfma_f32_16x16x32_bf16 v[102:105], v[174:177], v[186:189], v[102:105]
	v_mfma_f32_16x16x32_bf16 v[90:93], v[166:169], v[194:197], v[90:93]
	v_mfma_f32_16x16x32_bf16 v[86:89], v[174:177], v[194:197], v[86:89]
	v_mfma_f32_16x16x32_bf16 v[82:85], v[166:169], v[224:227], v[82:85]
	v_mfma_f32_16x16x32_bf16 v[78:81], v[174:177], v[224:227], v[78:81]
	v_mfma_f32_16x16x32_bf16 v[74:77], v[166:169], v[232:235], v[74:77]
	v_mfma_f32_16x16x32_bf16 v[70:73], v[174:177], v[232:235], v[70:73]
	v_mfma_f32_16x16x32_bf16 v[106:109], v[170:173], v[190:193], v[106:109]
	v_mfma_f32_16x16x32_bf16 v[102:105], v[178:181], v[190:193], v[102:105]
	v_mfma_f32_16x16x32_bf16 v[90:93], v[170:173], v[198:201], v[90:93]
	v_mfma_f32_16x16x32_bf16 v[86:89], v[178:181], v[198:201], v[86:89]
	v_mfma_f32_16x16x32_bf16 v[82:85], v[170:173], v[228:231], v[82:85]
	v_mfma_f32_16x16x32_bf16 v[78:81], v[178:181], v[228:231], v[78:81]
	v_mfma_f32_16x16x32_bf16 v[74:77], v[170:173], v[236:239], v[74:77]
	v_mfma_f32_16x16x32_bf16 v[70:73], v[178:181], v[236:239], v[70:73]
	s_setprio 0
	s_barrier
	s_add_i32 s22, s33, s31
	v_lshl_add_u64 v[182:183], v[182:183], 0, s[46:47]
	s_mov_b32 m0, s22
	ds_read_b128 v[186:189], v165 offset:49152
	ds_read_b128 v[190:193], v165 offset:50176
	ds_read_b128 v[194:197], v165 offset:51200
	ds_read_b128 v[198:201], v165 offset:52224
	ds_read_b128 v[224:227], v165 offset:53248
	ds_read_b128 v[228:231], v165 offset:54272
	ds_read_b128 v[232:235], v165 offset:55296
	ds_read_b128 v[236:239], v165 offset:56320
	global_load_lds_dwordx4 v[182:183], off
	s_add_i32 m0, s22, 0x2000
	s_add_u32 s20, s20, 0x40080
	v_lshl_add_u64 v[182:183], v[184:185], 0, s[46:47]
	s_addc_u32 s21, s21, 0
	s_add_i32 s22, s40, s31
	global_load_lds_dwordx4 v[182:183], off
	v_lshl_add_u64 v[182:183], s[20:21], 0, v[0:1]
	s_mov_b32 m0, s22
	s_nop 0
	global_load_lds_dwordx4 v[182:183], off
	v_lshl_add_u64 v[182:183], s[20:21], 0, v[134:135]
	s_add_i32 m0, s22, 0x2000
	s_nop 0
	global_load_lds_dwordx4 v[182:183], off
	v_lshl_add_u64 v[182:183], v[202:203], 0, s[46:47]
	s_mov_b32 m0, s38
	s_nop 0
	global_load_lds_dwordx4 v[182:183], off
	v_lshl_add_u64 v[182:183], v[210:211], 0, s[46:47]
	s_mov_b32 m0, s39
	s_nop 0
	global_load_lds_dwordx4 v[182:183], off
	s_waitcnt vmcnt(8)
	s_waitcnt lgkmcnt(0)
	s_barrier
	s_setprio 1
	s_waitcnt lgkmcnt(0)
	v_mfma_f32_16x16x32_bf16 v[66:69], v[146:149], v[186:189], v[66:69]
	v_mfma_f32_16x16x32_bf16 v[62:65], v[154:157], v[186:189], v[62:65]
	v_mfma_f32_16x16x32_bf16 v[58:61], v[146:149], v[194:197], v[58:61]
	v_mfma_f32_16x16x32_bf16 v[54:57], v[154:157], v[194:197], v[54:57]
	v_mfma_f32_16x16x32_bf16 v[50:53], v[146:149], v[224:227], v[50:53]
	v_mfma_f32_16x16x32_bf16 v[46:49], v[154:157], v[224:227], v[46:49]
	v_mfma_f32_16x16x32_bf16 v[30:33], v[146:149], v[232:235], v[30:33]
	v_mfma_f32_16x16x32_bf16 v[26:29], v[154:157], v[232:235], v[26:29]
	v_mfma_f32_16x16x32_bf16 v[66:69], v[150:153], v[190:193], v[66:69]
	v_mfma_f32_16x16x32_bf16 v[62:65], v[158:161], v[190:193], v[62:65]
	v_mfma_f32_16x16x32_bf16 v[58:61], v[150:153], v[198:201], v[58:61]
	v_mfma_f32_16x16x32_bf16 v[54:57], v[158:161], v[198:201], v[54:57]
	v_mfma_f32_16x16x32_bf16 v[50:53], v[150:153], v[228:231], v[50:53]
	v_mfma_f32_16x16x32_bf16 v[46:49], v[158:161], v[228:231], v[46:49]
	v_mfma_f32_16x16x32_bf16 v[30:33], v[150:153], v[236:239], v[30:33]
	v_mfma_f32_16x16x32_bf16 v[26:29], v[158:161], v[236:239], v[26:29]
	s_setprio 0
	s_setprio 1
	v_mfma_f32_16x16x32_bf16 v[42:45], v[166:169], v[186:189], v[42:45]
	v_mfma_f32_16x16x32_bf16 v[38:41], v[174:177], v[186:189], v[38:41]
	v_mfma_f32_16x16x32_bf16 v[22:25], v[166:169], v[194:197], v[22:25]
	v_mfma_f32_16x16x32_bf16 v[18:21], v[174:177], v[194:197], v[18:21]
	v_mfma_f32_16x16x32_bf16 v[14:17], v[166:169], v[224:227], v[14:17]
	v_mfma_f32_16x16x32_bf16 v[10:13], v[174:177], v[224:227], v[10:13]
	v_mfma_f32_16x16x32_bf16 v[6:9], v[166:169], v[232:235], v[6:9]
	v_mfma_f32_16x16x32_bf16 v[2:5], v[174:177], v[232:235], v[2:5]
	v_mfma_f32_16x16x32_bf16 v[42:45], v[170:173], v[190:193], v[42:45]
	v_mfma_f32_16x16x32_bf16 v[38:41], v[178:181], v[190:193], v[38:41]
	v_mfma_f32_16x16x32_bf16 v[22:25], v[170:173], v[198:201], v[22:25]
	v_mfma_f32_16x16x32_bf16 v[18:21], v[178:181], v[198:201], v[18:21]
	v_mfma_f32_16x16x32_bf16 v[14:17], v[170:173], v[228:231], v[14:17]
	v_mfma_f32_16x16x32_bf16 v[10:13], v[178:181], v[228:231], v[10:13]
	v_mfma_f32_16x16x32_bf16 v[6:9], v[170:173], v[236:239], v[6:9]
	v_mfma_f32_16x16x32_bf16 v[2:5], v[178:181], v[236:239], v[2:5]
	s_setprio 0
	s_barrier
	s_add_i32 s55, s55, 2
	s_add_u32 s53, s53, 0x100
	s_addc_u32 s54, s54, 0
	s_add_u32 s18, s18, 0x100
	s_addc_u32 s19, s19, 0

.LBB0_140:
	v_lshl_or_b32 v148, s50, 8, v164
	v_lshl_add_u32 v146, s14, 8, v162
	v_ashrrev_i32_e32 v149, 31, v148
	v_mov_b64_e32 v[170:171], s[4:5]
	s_movk_i32 s9, 0x1c00
	v_mad_i64_i32 v[150:151], s[18:19], v146, s9, v[170:171]
	v_lshlrev_b64 v[172:173], 1, v[148:149]
	v_lshl_add_u64 v[152:153], v[150:151], 0, v[172:173]
	v_cvt_pk_bf16_f32 v148, v130, v131
	v_cvt_pk_bf16_f32 v149, v132, v133
	v_cvt_pk_bf16_f32 v150, v126, v127
	v_cvt_pk_bf16_f32 v151, v128, v129
	global_store_dwordx4 v[152:153], v[148:151], off
	v_cvt_pk_bf16_f32 v168, v46, v47
	v_cvt_pk_bf16_f32 v169, v48, v49
	v_cvt_pk_bf16_f32 v148, v106, v107
	v_cvt_pk_bf16_f32 v149, v108, v109
	v_cvt_pk_bf16_f32 v150, v102, v103
	v_cvt_pk_bf16_f32 v151, v104, v105
	global_store_dwordx4 v[152:153], v[148:151], off offset:256
	v_cvt_pk_bf16_f32 v152, v118, v119
	v_cvt_pk_bf16_f32 v153, v120, v121
	v_or_b32_e32 v148, 16, v146
	v_mad_i64_i32 v[150:151], s[18:19], v148, s9, v[170:171]
	v_lshl_add_u64 v[154:155], v[150:151], 0, v[172:173]
	v_cvt_pk_bf16_f32 v150, v122, v123
	v_cvt_pk_bf16_f32 v151, v124, v125
	global_store_dwordx4 v[154:155], v[150:153], off
	s_cmp_lg_u32 s50, 13
	s_nop 0
	v_cvt_pk_bf16_f32 v150, v90, v91
	v_cvt_pk_bf16_f32 v151, v92, v93
	v_cvt_pk_bf16_f32 v152, v86, v87
	v_cvt_pk_bf16_f32 v153, v88, v89
	global_store_dwordx4 v[154:155], v[150:153], off offset:256
	v_cvt_pk_bf16_f32 v154, v110, v111
	v_cvt_pk_bf16_f32 v155, v112, v113
	v_or_b32_e32 v150, 32, v146
	v_mad_i64_i32 v[152:153], s[18:19], v150, s9, v[170:171]
	v_lshl_add_u64 v[156:157], v[152:153], 0, v[172:173]
	v_cvt_pk_bf16_f32 v152, v114, v115
	v_cvt_pk_bf16_f32 v153, v116, v117
	global_store_dwordx4 v[156:157], v[152:155], off
	s_nop 1
	v_cvt_pk_bf16_f32 v152, v82, v83
	v_cvt_pk_bf16_f32 v153, v84, v85
	v_cvt_pk_bf16_f32 v154, v78, v79
	v_cvt_pk_bf16_f32 v155, v80, v81
	global_store_dwordx4 v[156:157], v[152:155], off offset:256
	v_cvt_pk_bf16_f32 v156, v94, v95
	v_cvt_pk_bf16_f32 v157, v96, v97
	v_or_b32_e32 v152, 48, v146
	v_mad_i64_i32 v[154:155], s[18:19], v152, s9, v[170:171]
	v_lshl_add_u64 v[158:159], v[154:155], 0, v[172:173]
	v_cvt_pk_bf16_f32 v154, v98, v99
	v_cvt_pk_bf16_f32 v155, v100, v101
	global_store_dwordx4 v[158:159], v[154:157], off
	s_nop 1
	v_cvt_pk_bf16_f32 v154, v74, v75
	v_cvt_pk_bf16_f32 v155, v76, v77
	v_cvt_pk_bf16_f32 v156, v70, v71
	v_cvt_pk_bf16_f32 v157, v72, v73
	global_store_dwordx4 v[158:159], v[154:157], off offset:256
	v_cvt_pk_bf16_f32 v158, v62, v63
	v_cvt_pk_bf16_f32 v159, v64, v65
	v_add_u32_e32 v154, 0x80, v146
	v_mad_i64_i32 v[156:157], s[18:19], v154, s9, v[170:171]
	v_lshl_add_u64 v[160:161], v[156:157], 0, v[172:173]
	v_cvt_pk_bf16_f32 v156, v66, v67
	v_cvt_pk_bf16_f32 v157, v68, v69
	global_store_dwordx4 v[160:161], v[156:159], off
	s_nop 1
	v_cvt_pk_bf16_f32 v156, v42, v43
	v_cvt_pk_bf16_f32 v157, v44, v45
	v_cvt_pk_bf16_f32 v158, v38, v39
	v_cvt_pk_bf16_f32 v159, v40, v41
	global_store_dwordx4 v[160:161], v[156:159], off offset:256
	v_cvt_pk_bf16_f32 v160, v54, v55
	v_cvt_pk_bf16_f32 v161, v56, v57
	v_add_u32_e32 v156, 0x90, v146
	v_mad_i64_i32 v[158:159], s[18:19], v156, s9, v[170:171]
	v_lshl_add_u64 v[166:167], v[158:159], 0, v[172:173]
	v_cvt_pk_bf16_f32 v158, v58, v59
	v_cvt_pk_bf16_f32 v159, v60, v61
	global_store_dwordx4 v[166:167], v[158:161], off
	s_nop 1
	v_cvt_pk_bf16_f32 v158, v22, v23
	v_cvt_pk_bf16_f32 v159, v24, v25
	v_cvt_pk_bf16_f32 v160, v18, v19
	v_cvt_pk_bf16_f32 v161, v20, v21
	global_store_dwordx4 v[166:167], v[158:161], off offset:256
	v_cvt_pk_bf16_f32 v166, v50, v51
	v_cvt_pk_bf16_f32 v167, v52, v53
	v_add_u32_e32 v158, 0xa0, v146
	v_mad_i64_i32 v[160:161], s[18:19], v158, s9, v[170:171]
	v_lshl_add_u64 v[160:161], v[160:161], 0, v[172:173]
	global_store_dwordx4 v[160:161], v[166:169], off
	s_nop 1
	v_cvt_pk_bf16_f32 v166, v14, v15
	v_cvt_pk_bf16_f32 v167, v16, v17
	v_cvt_pk_bf16_f32 v168, v10, v11
	v_cvt_pk_bf16_f32 v169, v12, v13
	global_store_dwordx4 v[160:161], v[166:169], off offset:256
	v_add_u32_e32 v160, 0xb0, v146
	s_nop 0
	v_mad_i64_i32 v[166:167], s[18:19], v160, s9, v[170:171]
	v_lshl_add_u64 v[170:171], v[166:167], 0, v[172:173]
	v_cvt_pk_bf16_f32 v166, v30, v31
	v_cvt_pk_bf16_f32 v167, v32, v33
	v_cvt_pk_bf16_f32 v168, v26, v27
	v_cvt_pk_bf16_f32 v169, v28, v29
	global_store_dwordx4 v[170:171], v[166:169], off
	s_nop 1
	v_cvt_pk_bf16_f32 v166, v6, v7
	v_cvt_pk_bf16_f32 v167, v8, v9
	v_cvt_pk_bf16_f32 v168, v2, v3
	v_cvt_pk_bf16_f32 v169, v4, v5
	global_store_dwordx4 v[170:171], v[166:169], off offset:256
	s_waitcnt vmcnt(16)
	s_mov_b32 s32, 1
	s_cbranch_scc1 .LBB0_142
	v_ashrrev_i32_e32 v147, 31, v146
	v_lshlrev_b64 v[146:147], 10, v[146:147]
	v_ashrrev_i32_e32 v149, 31, v148
	v_lshl_add_u64 v[146:147], v[140:141], 0, v[146:147]
	global_store_dwordx4 v[146:147], v[130:133], off
	global_store_dwordx4 v[146:147], v[126:129], off offset:16
	global_store_dwordx4 v[146:147], v[106:109], off offset:512
	global_store_dwordx4 v[146:147], v[102:105], off offset:528
	v_ashrrev_i32_e32 v151, 31, v150
	v_ashrrev_i32_e32 v153, 31, v152
	v_lshlrev_b64 v[102:103], 10, v[148:149]
	v_lshl_add_u64 v[102:103], v[140:141], 0, v[102:103]
	global_store_dwordx4 v[102:103], v[122:125], off
	global_store_dwordx4 v[102:103], v[118:121], off offset:16
	global_store_dwordx4 v[102:103], v[90:93], off offset:512
	global_store_dwordx4 v[102:103], v[86:89], off offset:528
	v_ashrrev_i32_e32 v155, 31, v154
	v_ashrrev_i32_e32 v157, 31, v156
	v_lshlrev_b64 v[86:87], 10, v[150:151]
	v_lshl_add_u64 v[86:87], v[140:141], 0, v[86:87]
	global_store_dwordx4 v[86:87], v[114:117], off
	global_store_dwordx4 v[86:87], v[110:113], off offset:16
	global_store_dwordx4 v[86:87], v[82:85], off offset:512
	global_store_dwordx4 v[86:87], v[78:81], off offset:528
	v_ashrrev_i32_e32 v159, 31, v158
	v_ashrrev_i32_e32 v161, 31, v160
	v_lshlrev_b64 v[78:79], 10, v[152:153]
	v_lshl_add_u64 v[78:79], v[140:141], 0, v[78:79]
	global_store_dwordx4 v[78:79], v[98:101], off
	global_store_dwordx4 v[78:79], v[94:97], off offset:16
	global_store_dwordx4 v[78:79], v[74:77], off offset:512
	global_store_dwordx4 v[78:79], v[70:73], off offset:528
	s_nop 1
	v_lshlrev_b64 v[70:71], 10, v[154:155]
	v_lshl_add_u64 v[70:71], v[140:141], 0, v[70:71]
	global_store_dwordx4 v[70:71], v[66:69], off
	global_store_dwordx4 v[70:71], v[62:65], off offset:16
	global_store_dwordx4 v[70:71], v[42:45], off offset:512
	global_store_dwordx4 v[70:71], v[38:41], off offset:528
	s_nop 1
	v_lshlrev_b64 v[38:39], 10, v[156:157]
	v_lshl_add_u64 v[38:39], v[140:141], 0, v[38:39]
	global_store_dwordx4 v[38:39], v[58:61], off
	global_store_dwordx4 v[38:39], v[54:57], off offset:16
	global_store_dwordx4 v[38:39], v[22:25], off offset:512
	global_store_dwordx4 v[38:39], v[18:21], off offset:528
	s_nop 1
	v_lshlrev_b64 v[18:19], 10, v[158:159]
	v_lshl_add_u64 v[18:19], v[140:141], 0, v[18:19]
	global_store_dwordx4 v[18:19], v[50:53], off
	global_store_dwordx4 v[18:19], v[46:49], off offset:16
	global_store_dwordx4 v[18:19], v[14:17], off offset:512
	global_store_dwordx4 v[18:19], v[10:13], off offset:528
	s_nop 1
	v_lshlrev_b64 v[10:11], 10, v[160:161]
	v_lshl_add_u64 v[10:11], v[140:141], 0, v[10:11]
	global_store_dwordx4 v[10:11], v[30:33], off
	global_store_dwordx4 v[10:11], v[26:29], off offset:16
	global_store_dwordx4 v[10:11], v[6:9], off offset:512
	global_store_dwordx4 v[10:11], v[2:5], off offset:528

.LBB0_2073:
	s_mov_b32 s32, 1
	v_lshl_add_u32 v0, s60, 8, v179
	v_ashrrev_i32_e32 v163, 31, v162
	v_lshlrev_b64 v[164:165], 11, v[162:163]
	v_lshl_add_u64 v[164:165], s[20:21], 0, v[164:165]
	v_lshlrev_b64 v[166:167], 1, v[0:1]
	v_lshl_add_u64 v[164:165], v[164:165], 0, v[166:167]
	s_mov_b32 s33, 0x40000
	s_mov_b64 s[40:41], 0x40000
	v_mov_b64_e32 v[134:135], v[206:207]
	v_mov_b64_e32 v[136:137], v[208:209]
	v_mov_b64_e32 v[142:143], v[34:35]
	v_mov_b64_e32 v[144:145], v[36:37]
	v_mov_b64_e32 v[146:147], v[212:213]
	v_mov_b64_e32 v[148:149], v[214:215]
	v_mov_b64_e32 v[138:139], v[216:217]
	v_mov_b64_e32 v[140:141], v[204:205]
	v_pk_add_f32 v[172:173], v[128:129], v[144:145]
	v_pk_add_f32 v[170:171], v[132:133], v[148:149]
	v_pk_add_f32 v[168:169], v[130:131], v[146:147]
	v_pk_add_f32 v[182:183], v[126:127], v[142:143]
	v_cvt_pk_bf16_f32 v168, v168, v169
	v_cvt_pk_bf16_f32 v169, v170, v171
	v_cvt_pk_bf16_f32 v170, v182, v183
	v_cvt_pk_bf16_f32 v171, v172, v173
	global_store_dwordx4 v[164:165], v[168:171], off
	v_pk_add_f32 v[172:173], v[96:97], v[136:137]
	v_pk_add_f32 v[182:183], v[94:95], v[134:135]
	v_pk_add_f32 v[170:171], v[100:101], v[140:141]
	v_pk_add_f32 v[168:169], v[98:99], v[138:139]
	v_pk_add_f32 v[184:185], v[118:119], v[142:143]
	v_cvt_pk_bf16_f32 v168, v168, v169
	v_cvt_pk_bf16_f32 v169, v170, v171
	v_cvt_pk_bf16_f32 v170, v182, v183
	v_cvt_pk_bf16_f32 v171, v172, v173
	global_store_dwordx4 v[164:165], v[168:171], off offset:256
	v_pk_add_f32 v[182:183], v[120:121], v[144:145]
	s_nop 0
	v_or_b32_e32 v168, 16, v162
	v_ashrrev_i32_e32 v169, 31, v168
	v_lshlrev_b64 v[168:169], 11, v[168:169]
	v_lshl_add_u64 v[168:169], s[20:21], 0, v[168:169]
	v_lshl_add_u64 v[172:173], v[168:169], 0, v[166:167]
	v_pk_add_f32 v[170:171], v[124:125], v[148:149]
	v_pk_add_f32 v[168:169], v[122:123], v[146:147]
	s_nop 0
	v_cvt_pk_bf16_f32 v168, v168, v169
	v_cvt_pk_bf16_f32 v169, v170, v171
	v_cvt_pk_bf16_f32 v170, v184, v185
	v_cvt_pk_bf16_f32 v171, v182, v183
	global_store_dwordx4 v[172:173], v[168:171], off
	v_pk_add_f32 v[182:183], v[88:89], v[136:137]
	v_pk_add_f32 v[184:185], v[86:87], v[134:135]
	v_pk_add_f32 v[170:171], v[92:93], v[140:141]
	v_pk_add_f32 v[168:169], v[90:91], v[138:139]
	s_nop 0
	v_cvt_pk_bf16_f32 v168, v168, v169
	v_cvt_pk_bf16_f32 v169, v170, v171
	v_cvt_pk_bf16_f32 v170, v184, v185
	v_cvt_pk_bf16_f32 v171, v182, v183
	global_store_dwordx4 v[172:173], v[168:171], off offset:256
	v_pk_add_f32 v[182:183], v[112:113], v[144:145]
	v_pk_add_f32 v[184:185], v[110:111], v[142:143]
	v_or_b32_e32 v168, 32, v162
	v_ashrrev_i32_e32 v169, 31, v168
	v_lshlrev_b64 v[168:169], 11, v[168:169]
	v_lshl_add_u64 v[168:169], s[20:21], 0, v[168:169]
	v_lshl_add_u64 v[172:173], v[168:169], 0, v[166:167]
	v_pk_add_f32 v[170:171], v[116:117], v[148:149]
	v_pk_add_f32 v[168:169], v[114:115], v[146:147]
	s_nop 0
	v_cvt_pk_bf16_f32 v168, v168, v169
	v_cvt_pk_bf16_f32 v169, v170, v171
	v_cvt_pk_bf16_f32 v170, v184, v185
	v_cvt_pk_bf16_f32 v171, v182, v183
	global_store_dwordx4 v[172:173], v[168:171], off
	v_pk_add_f32 v[182:183], v[80:81], v[136:137]
	v_pk_add_f32 v[184:185], v[78:79], v[134:135]
	v_pk_add_f32 v[170:171], v[84:85], v[140:141]
	v_pk_add_f32 v[168:169], v[82:83], v[138:139]
	s_nop 0
	v_cvt_pk_bf16_f32 v168, v168, v169
	v_cvt_pk_bf16_f32 v169, v170, v171
	v_cvt_pk_bf16_f32 v170, v184, v185
	v_cvt_pk_bf16_f32 v171, v182, v183
	global_store_dwordx4 v[172:173], v[168:171], off offset:256
	v_pk_add_f32 v[172:173], v[104:105], v[144:145]
	v_pk_add_f32 v[182:183], v[102:103], v[142:143]
	v_or_b32_e32 v168, 48, v162
	v_ashrrev_i32_e32 v169, 31, v168
	v_lshlrev_b64 v[168:169], 11, v[168:169]
	v_lshl_add_u64 v[168:169], s[20:21], 0, v[168:169]
	v_lshl_add_u64 v[170:171], v[168:169], 0, v[166:167]
	v_pk_add_f32 v[168:169], v[108:109], v[148:149]
	v_pk_add_f32 v[166:167], v[106:107], v[146:147]
	s_nop 0
	v_cvt_pk_bf16_f32 v166, v166, v167
	v_cvt_pk_bf16_f32 v167, v168, v169
	v_cvt_pk_bf16_f32 v168, v182, v183
	v_cvt_pk_bf16_f32 v169, v172, v173
	global_store_dwordx4 v[170:171], v[166:169], off
	v_pk_add_f32 v[172:173], v[72:73], v[136:137]
	v_pk_add_f32 v[182:183], v[70:71], v[134:135]
	v_pk_add_f32 v[168:169], v[76:77], v[140:141]
	v_pk_add_f32 v[166:167], v[74:75], v[138:139]
	s_nop 0
	v_cvt_pk_bf16_f32 v166, v166, v167
	v_cvt_pk_bf16_f32 v167, v168, v169
	v_cvt_pk_bf16_f32 v168, v182, v183
	v_cvt_pk_bf16_f32 v169, v172, v173
	global_store_dwordx4 v[170:171], v[166:169], off offset:256
	v_pk_add_f32 v[172:173], v[64:65], v[144:145]
	v_pk_add_f32 v[182:183], v[62:63], v[142:143]
	v_pk_add_f32 v[168:169], v[68:69], v[148:149]
	v_pk_add_f32 v[166:167], v[66:67], v[146:147]
	v_lshl_add_u64 v[170:171], v[164:165], 0, s[40:41]
	v_cvt_pk_bf16_f32 v166, v166, v167
	v_cvt_pk_bf16_f32 v167, v168, v169
	v_cvt_pk_bf16_f32 v169, v172, v173
	v_add_co_u32_e32 v172, vcc, s33, v164
	v_cvt_pk_bf16_f32 v168, v182, v183
	s_nop 0
	v_addc_co_u32_e32 v173, vcc, 0, v165, vcc
	global_store_dwordx4 v[172:173], v[166:169], off
	v_pk_add_f32 v[172:173], v[28:29], v[136:137]
	v_pk_add_f32 v[182:183], v[26:27], v[134:135]
	v_pk_add_f32 v[168:169], v[32:33], v[140:141]
	v_pk_add_f32 v[166:167], v[30:31], v[138:139]
	s_mov_b32 s33, 0x48000
	v_cvt_pk_bf16_f32 v166, v166, v167
	v_cvt_pk_bf16_f32 v167, v168, v169
	v_cvt_pk_bf16_f32 v168, v182, v183
	v_cvt_pk_bf16_f32 v169, v172, v173
	global_store_dwordx4 v[170:171], v[166:169], off offset:256
	v_pk_add_f32 v[172:173], v[56:57], v[144:145]
	v_pk_add_f32 v[182:183], v[54:55], v[142:143]
	v_pk_add_f32 v[168:169], v[60:61], v[148:149]
	v_pk_add_f32 v[166:167], v[58:59], v[146:147]
	s_mov_b64 s[40:41], 0x48000
	v_cvt_pk_bf16_f32 v166, v166, v167
	v_cvt_pk_bf16_f32 v167, v168, v169
	v_cvt_pk_bf16_f32 v169, v172, v173
	v_add_co_u32_e32 v172, vcc, s33, v164
	v_cvt_pk_bf16_f32 v168, v182, v183
	s_nop 0
	v_addc_co_u32_e32 v173, vcc, 0, v165, vcc
	global_store_dwordx4 v[172:173], v[166:169], off
	v_pk_add_f32 v[172:173], v[20:21], v[136:137]
	v_pk_add_f32 v[182:183], v[18:19], v[134:135]
	v_pk_add_f32 v[168:169], v[24:25], v[140:141]
	v_pk_add_f32 v[166:167], v[22:23], v[138:139]
	v_lshl_add_u64 v[170:171], v[164:165], 0, s[40:41]
	v_cvt_pk_bf16_f32 v166, v166, v167
	v_cvt_pk_bf16_f32 v167, v168, v169
	v_cvt_pk_bf16_f32 v168, v182, v183
	v_cvt_pk_bf16_f32 v169, v172, v173
	global_store_dwordx4 v[170:171], v[166:169], off offset:256
	v_pk_add_f32 v[172:173], v[48:49], v[144:145]
	s_mov_b32 s33, 0x50000
	v_pk_add_f32 v[168:169], v[52:53], v[148:149]
	v_pk_add_f32 v[166:167], v[50:51], v[146:147]
	v_pk_add_f32 v[182:183], v[46:47], v[142:143]
	v_cvt_pk_bf16_f32 v166, v166, v167
	v_cvt_pk_bf16_f32 v167, v168, v169
	v_cvt_pk_bf16_f32 v169, v172, v173
	v_add_co_u32_e32 v172, vcc, s33, v164
	v_cvt_pk_bf16_f32 v168, v182, v183
	s_nop 0
	v_addc_co_u32_e32 v173, vcc, 0, v165, vcc
	s_mov_b64 s[40:41], 0x50000
	global_store_dwordx4 v[172:173], v[166:169], off
	v_pk_add_f32 v[172:173], v[12:13], v[136:137]
	v_pk_add_f32 v[182:183], v[10:11], v[134:135]
	v_pk_add_f32 v[168:169], v[16:17], v[140:141]
	v_pk_add_f32 v[166:167], v[14:15], v[138:139]
	v_lshl_add_u64 v[170:171], v[164:165], 0, s[40:41]
	v_cvt_pk_bf16_f32 v166, v166, v167
	v_cvt_pk_bf16_f32 v167, v168, v169
	v_cvt_pk_bf16_f32 v168, v182, v183
	v_cvt_pk_bf16_f32 v169, v172, v173
	v_pk_add_f32 v[146:147], v[42:43], v[146:147]
	s_mov_b32 s33, 0x58000
	global_store_dwordx4 v[170:171], v[166:169], off offset:256
	v_pk_add_f32 v[148:149], v[44:45], v[148:149]
	s_mov_b64 s[40:41], 0x58000
	v_pk_add_f32 v[168:169], v[40:41], v[144:145]
	v_pk_add_f32 v[144:145], v[38:39], v[142:143]
	v_cvt_pk_bf16_f32 v142, v146, v147
	v_add_co_u32_e32 v146, vcc, s33, v164
	v_cvt_pk_bf16_f32 v143, v148, v149
	v_cvt_pk_bf16_f32 v144, v144, v145
	v_cvt_pk_bf16_f32 v145, v168, v169
	v_addc_co_u32_e32 v147, vcc, 0, v165, vcc
	global_store_dwordx4 v[146:147], v[142:145], off
	v_pk_add_f32 v[140:141], v[8:9], v[140:141]
	v_pk_add_f32 v[138:139], v[6:7], v[138:139]
	v_pk_add_f32 v[142:143], v[4:5], v[136:137]
	v_pk_add_f32 v[136:137], v[2:3], v[134:135]
	v_lshl_add_u64 v[166:167], v[164:165], 0, s[40:41]
	v_cvt_pk_bf16_f32 v134, v138, v139
	v_cvt_pk_bf16_f32 v135, v140, v141
	v_cvt_pk_bf16_f32 v136, v136, v137
	v_cvt_pk_bf16_f32 v137, v142, v143
	global_store_dwordx4 v[166:167], v[134:137], off offset:256
	s_waitcnt vmcnt(16)
	s_mov_b32 s50, -1
	s_cbranch_execnz .LBB0_2069
.LBB0_2074:
	s_mov_b32 s32, 1
	v_lshl_or_b32 v0, s60, 7, v178
	s_mov_b32 s13, 0xc0e00000
	v_lshlrev_b32_e32 v0, 1, v0
	v_lshl_add_u32 v0, v162, 11, v0
	v_readlane_b32 s40, v252, 29
	v_readlane_b32 s41, v252, 30
	v_readlane_b32 s42, v252, 31
	v_readlane_b32 s43, v252, 32
	s_mov_b32 s50, s10
	v_mov_b64_e32 v[134:135], v[206:207]
	v_mov_b64_e32 v[136:137], v[208:209]
	v_mov_b64_e32 v[142:143], v[34:35]
	v_mov_b64_e32 v[144:145], v[36:37]
	v_mov_b64_e32 v[146:147], v[212:213]
	v_mov_b64_e32 v[148:149], v[214:215]
	v_mov_b64_e32 v[138:139], v[216:217]
	v_mov_b64_e32 v[140:141], v[204:205]
	v_add_f32_e32 v155, v130, v142
	v_min_f32_e32 v164, 0x40e00000, v155
	v_mul_f32_e32 v155, 0xbfd9db23, v164
	v_mul_f32_e32 v155, 0x3fb8aa3b, v155
	v_exp_f32_e32 v155, v155
	v_add_f32_e32 v161, v98, v146
	v_add_f32_e32 v155, 1.0, v155
	v_rcp_f32_e32 v168, v155
	v_add_f32_e32 v155, v131, v143
	v_min_f32_e32 v165, 0x40e00000, v155
	v_mul_f32_e32 v155, 0xbfd9db23, v165
	v_mul_f32_e32 v155, 0x3fb8aa3b, v155
	v_exp_f32_e32 v155, v155
	v_med3_f32 v166, v161, s13, v222
	v_add_f32_e32 v161, v99, v147
	v_med3_f32 v167, v161, s13, v222
	v_add_f32_e32 v155, 1.0, v155
	v_rcp_f32_e32 v169, v155
	v_pk_add_f32 v[166:167], v[166:167], 1.0 op_sel_hi:[1,0]
	v_add_f32_e32 v155, v132, v144
	v_add_f32_e32 v161, v100, v148
	v_pk_mul_f32 v[164:165], v[164:165], v[168:169]
	v_med3_f32 v168, v161, s13, v222
	v_pk_mul_f32 v[164:165], v[166:167], v[164:165]
	v_min_f32_e32 v166, 0x40e00000, v155
	v_mul_f32_e32 v155, 0xbfd9db23, v166
	v_mul_f32_e32 v155, 0x3fb8aa3b, v155
	v_exp_f32_e32 v155, v155
	v_add_f32_e32 v161, v101, v149
	v_med3_f32 v169, v161, s13, v222
	v_pk_add_f32 v[168:169], v[168:169], 1.0 op_sel_hi:[1,0]
	v_add_f32_e32 v155, 1.0, v155
	v_rcp_f32_e32 v170, v155
	v_add_f32_e32 v155, v133, v145
	v_min_f32_e32 v167, 0x40e00000, v155
	v_mul_f32_e32 v155, 0xbfd9db23, v167
	v_mul_f32_e32 v155, 0x3fb8aa3b, v155
	v_exp_f32_e32 v155, v155
	v_add_f32_e32 v161, v94, v138
	v_cvt_pk_bf16_f32 v164, v164, v165
	v_add_f32_e32 v155, 1.0, v155
	v_rcp_f32_e32 v171, v155
	v_add_f32_e32 v155, v126, v134
	v_pk_mul_f32 v[166:167], v[166:167], v[170:171]
	s_nop 0
	v_pk_mul_f32 v[166:167], v[168:169], v[166:167]
	v_min_f32_e32 v168, 0x40e00000, v155
	v_mul_f32_e32 v155, 0xbfd9db23, v168
	v_mul_f32_e32 v155, 0x3fb8aa3b, v155
	v_exp_f32_e32 v155, v155
	v_med3_f32 v170, v161, s13, v222
	v_add_f32_e32 v161, v95, v139
	v_med3_f32 v171, v161, s13, v222
	v_add_f32_e32 v155, 1.0, v155
	v_rcp_f32_e32 v172, v155
	v_add_f32_e32 v155, v127, v135
	v_min_f32_e32 v169, 0x40e00000, v155
	v_mul_f32_e32 v155, 0xbfd9db23, v169
	v_mul_f32_e32 v155, 0x3fb8aa3b, v155
	v_exp_f32_e32 v155, v155
	v_pk_add_f32 v[170:171], v[170:171], 1.0 op_sel_hi:[1,0]
	v_add_f32_e32 v161, v96, v140
	v_med3_f32 v182, v161, s13, v222
	v_add_f32_e32 v155, 1.0, v155
	v_rcp_f32_e32 v173, v155
	v_add_f32_e32 v155, v128, v136
	v_add_f32_e32 v161, v97, v141
	v_med3_f32 v183, v161, s13, v222
	v_pk_mul_f32 v[168:169], v[168:169], v[172:173]
	v_pk_add_f32 v[182:183], v[182:183], 1.0 op_sel_hi:[1,0]
	v_pk_mul_f32 v[168:169], v[170:171], v[168:169]
	v_min_f32_e32 v170, 0x40e00000, v155
	v_mul_f32_e32 v155, 0xbfd9db23, v170
	v_mul_f32_e32 v155, 0x3fb8aa3b, v155
	v_exp_f32_e32 v155, v155
	v_cvt_pk_bf16_f32 v165, v166, v167
	v_cvt_pk_bf16_f32 v166, v168, v169
	v_add_f32_e32 v161, v90, v146
	v_add_f32_e32 v155, 1.0, v155
	v_rcp_f32_e32 v172, v155
	v_add_f32_e32 v155, v129, v137
	v_min_f32_e32 v171, 0x40e00000, v155
	v_mul_f32_e32 v155, 0xbfd9db23, v171
	v_mul_f32_e32 v155, 0x3fb8aa3b, v155
	v_exp_f32_e32 v155, v155
	s_nop 0
	v_add_f32_e32 v155, 1.0, v155
	v_rcp_f32_e32 v173, v155
	v_add_f32_e32 v155, v122, v142
	v_min_f32_e32 v162, 0x40e00000, v155
	v_mul_f32_e32 v155, 0xbfd9db23, v162
	v_mul_f32_e32 v155, 0x3fb8aa3b, v155
	v_exp_f32_e32 v155, v155
	v_pk_mul_f32 v[170:171], v[170:171], v[172:173]
	v_add_f32_e32 v155, 1.0, v155
	v_pk_mul_f32 v[170:171], v[182:183], v[170:171]
	s_nop 0
	v_cvt_pk_bf16_f32 v167, v170, v171
	buffer_store_dwordx4 v[164:167], v0, s[40:43], 0 offen sc1
	s_nop 1
	v_rcp_f32_e32 v166, v155
	v_add_f32_e32 v155, v123, v143
	v_min_f32_e32 v163, 0x40e00000, v155
	v_mul_f32_e32 v155, 0xbfd9db23, v163
	v_mul_f32_e32 v155, 0x3fb8aa3b, v155
	v_exp_f32_e32 v155, v155
	v_med3_f32 v164, v161, s13, v222
	v_add_f32_e32 v161, v91, v147
	v_med3_f32 v165, v161, s13, v222
	v_add_f32_e32 v155, 1.0, v155
	v_rcp_f32_e32 v167, v155
	v_pk_add_f32 v[164:165], v[164:165], 1.0 op_sel_hi:[1,0]
	v_add_f32_e32 v155, v124, v144
	v_add_f32_e32 v161, v92, v148
	v_pk_mul_f32 v[162:163], v[162:163], v[166:167]
	v_med3_f32 v166, v161, s13, v222
	v_pk_mul_f32 v[162:163], v[164:165], v[162:163]
	v_min_f32_e32 v164, 0x40e00000, v155
	v_mul_f32_e32 v155, 0xbfd9db23, v164
	v_mul_f32_e32 v155, 0x3fb8aa3b, v155
	v_exp_f32_e32 v155, v155
	v_add_f32_e32 v161, v93, v149
	v_med3_f32 v167, v161, s13, v222
	v_pk_add_f32 v[166:167], v[166:167], 1.0 op_sel_hi:[1,0]
	v_add_f32_e32 v155, 1.0, v155
	v_rcp_f32_e32 v168, v155
	v_add_f32_e32 v155, v125, v145
	v_min_f32_e32 v165, 0x40e00000, v155
	v_mul_f32_e32 v155, 0xbfd9db23, v165
	v_mul_f32_e32 v155, 0x3fb8aa3b, v155
	v_exp_f32_e32 v155, v155
	v_add_f32_e32 v161, v86, v138
	v_cvt_pk_bf16_f32 v162, v162, v163
	v_add_f32_e32 v155, 1.0, v155
	v_rcp_f32_e32 v169, v155
	v_add_f32_e32 v155, v118, v134
	v_pk_mul_f32 v[164:165], v[164:165], v[168:169]
	s_nop 0
	v_pk_mul_f32 v[164:165], v[166:167], v[164:165]
	v_min_f32_e32 v166, 0x40e00000, v155
	v_mul_f32_e32 v155, 0xbfd9db23, v166
	v_mul_f32_e32 v155, 0x3fb8aa3b, v155
	v_exp_f32_e32 v155, v155
	v_med3_f32 v168, v161, s13, v222
	v_add_f32_e32 v161, v87, v139
	v_med3_f32 v169, v161, s13, v222
	v_add_f32_e32 v155, 1.0, v155
	v_rcp_f32_e32 v170, v155
	v_add_f32_e32 v155, v119, v135
	v_min_f32_e32 v167, 0x40e00000, v155
	v_mul_f32_e32 v155, 0xbfd9db23, v167
	v_mul_f32_e32 v155, 0x3fb8aa3b, v155
	v_exp_f32_e32 v155, v155
	v_pk_add_f32 v[168:169], v[168:169], 1.0 op_sel_hi:[1,0]
	v_add_f32_e32 v161, v88, v140
	v_cvt_pk_bf16_f32 v163, v164, v165
	v_add_f32_e32 v155, 1.0, v155
	v_rcp_f32_e32 v171, v155
	v_add_f32_e32 v155, v120, v136
	v_pk_mul_f32 v[166:167], v[166:167], v[170:171]
	s_nop 0
	v_pk_mul_f32 v[166:167], v[168:169], v[166:167]
	v_min_f32_e32 v168, 0x40e00000, v155
	v_mul_f32_e32 v155, 0xbfd9db23, v168
	v_mul_f32_e32 v155, 0x3fb8aa3b, v155
	v_exp_f32_e32 v155, v155
	v_med3_f32 v170, v161, s13, v222
	v_add_f32_e32 v161, v89, v141
	v_med3_f32 v171, v161, s13, v222
	v_add_f32_e32 v155, 1.0, v155
	v_rcp_f32_e32 v172, v155
	v_add_f32_e32 v155, v121, v137
	v_min_f32_e32 v169, 0x40e00000, v155
	v_mul_f32_e32 v155, 0xbfd9db23, v169
	v_mul_f32_e32 v155, 0x3fb8aa3b, v155
	v_exp_f32_e32 v155, v155
	v_pk_add_f32 v[170:171], v[170:171], 1.0 op_sel_hi:[1,0]
	v_cvt_pk_bf16_f32 v164, v166, v167
	v_add_f32_e32 v161, v82, v146
	v_add_f32_e32 v155, 1.0, v155
	v_rcp_f32_e32 v173, v155
	v_add_u32_e32 v155, 0x8000, v0
	v_pk_mul_f32 v[168:169], v[168:169], v[172:173]
	s_nop 0
	v_pk_mul_f32 v[168:169], v[170:171], v[168:169]
	s_nop 0
	v_cvt_pk_bf16_f32 v165, v168, v169
	buffer_store_dwordx4 v[162:165], v155, s[40:43], 0 offen sc1
	v_add_f32_e32 v155, v114, v142
	s_nop 0
	v_min_f32_e32 v162, 0x40e00000, v155
	v_mul_f32_e32 v155, 0xbfd9db23, v162
	v_mul_f32_e32 v155, 0x3fb8aa3b, v155
	v_exp_f32_e32 v155, v155
	v_med3_f32 v164, v161, s13, v222
	v_add_f32_e32 v161, v83, v147
	v_med3_f32 v165, v161, s13, v222
	v_add_f32_e32 v155, 1.0, v155
	v_rcp_f32_e32 v166, v155
	v_add_f32_e32 v155, v115, v143
	v_min_f32_e32 v163, 0x40e00000, v155
	v_mul_f32_e32 v155, 0xbfd9db23, v163
	v_mul_f32_e32 v155, 0x3fb8aa3b, v155
	v_exp_f32_e32 v155, v155
	v_pk_add_f32 v[164:165], v[164:165], 1.0 op_sel_hi:[1,0]
	v_add_f32_e32 v161, v84, v148
	v_add_f32_e32 v155, 1.0, v155
	v_rcp_f32_e32 v167, v155
	v_add_f32_e32 v155, v116, v144
	v_pk_mul_f32 v[162:163], v[162:163], v[166:167]
	s_nop 0
	v_pk_mul_f32 v[162:163], v[164:165], v[162:163]
	v_min_f32_e32 v164, 0x40e00000, v155
	v_mul_f32_e32 v155, 0xbfd9db23, v164
	v_mul_f32_e32 v155, 0x3fb8aa3b, v155
	v_exp_f32_e32 v155, v155
	v_med3_f32 v166, v161, s13, v222
	v_add_f32_e32 v161, v85, v149
	v_med3_f32 v167, v161, s13, v222
	v_add_f32_e32 v155, 1.0, v155
	v_rcp_f32_e32 v168, v155
	v_add_f32_e32 v155, v117, v145
	v_min_f32_e32 v165, 0x40e00000, v155
	v_mul_f32_e32 v155, 0xbfd9db23, v165
	v_mul_f32_e32 v155, 0x3fb8aa3b, v155
	v_exp_f32_e32 v155, v155
	v_pk_add_f32 v[166:167], v[166:167], 1.0 op_sel_hi:[1,0]
	v_add_f32_e32 v161, v78, v138
	v_cvt_pk_bf16_f32 v162, v162, v163
	v_add_f32_e32 v155, 1.0, v155
	v_rcp_f32_e32 v169, v155
	v_add_f32_e32 v155, v110, v134
	v_pk_mul_f32 v[164:165], v[164:165], v[168:169]
	s_nop 0
	v_pk_mul_f32 v[164:165], v[166:167], v[164:165]
	v_min_f32_e32 v166, 0x40e00000, v155
	v_mul_f32_e32 v155, 0xbfd9db23, v166
	v_mul_f32_e32 v155, 0x3fb8aa3b, v155
	v_exp_f32_e32 v155, v155
	v_med3_f32 v168, v161, s13, v222
	v_add_f32_e32 v161, v79, v139
	v_med3_f32 v169, v161, s13, v222
	v_add_f32_e32 v155, 1.0, v155
	v_rcp_f32_e32 v170, v155
	v_add_f32_e32 v155, v111, v135
	v_min_f32_e32 v167, 0x40e00000, v155
	v_mul_f32_e32 v155, 0xbfd9db23, v167
	v_mul_f32_e32 v155, 0x3fb8aa3b, v155
	v_exp_f32_e32 v155, v155
	v_pk_add_f32 v[168:169], v[168:169], 1.0 op_sel_hi:[1,0]
	v_add_f32_e32 v161, v80, v140
	v_cvt_pk_bf16_f32 v163, v164, v165
	v_add_f32_e32 v155, 1.0, v155
	v_rcp_f32_e32 v171, v155
	v_add_f32_e32 v155, v112, v136
	v_pk_mul_f32 v[166:167], v[166:167], v[170:171]
	s_nop 0
	v_pk_mul_f32 v[166:167], v[168:169], v[166:167]
	v_min_f32_e32 v168, 0x40e00000, v155
	v_mul_f32_e32 v155, 0xbfd9db23, v168
	v_mul_f32_e32 v155, 0x3fb8aa3b, v155
	v_exp_f32_e32 v155, v155
	v_med3_f32 v170, v161, s13, v222
	v_add_f32_e32 v161, v81, v141
	v_med3_f32 v171, v161, s13, v222
	v_add_f32_e32 v155, 1.0, v155
	v_rcp_f32_e32 v172, v155
	v_add_f32_e32 v155, v113, v137
	v_min_f32_e32 v169, 0x40e00000, v155
	v_mul_f32_e32 v155, 0xbfd9db23, v169
	v_mul_f32_e32 v155, 0x3fb8aa3b, v155
	v_exp_f32_e32 v155, v155
	v_pk_add_f32 v[170:171], v[170:171], 1.0 op_sel_hi:[1,0]
	v_cvt_pk_bf16_f32 v164, v166, v167
	v_add_f32_e32 v161, v74, v146
	v_add_f32_e32 v155, 1.0, v155
	v_rcp_f32_e32 v173, v155
	v_add_u32_e32 v155, 0x10000, v0
	v_pk_mul_f32 v[168:169], v[168:169], v[172:173]
	s_nop 0
	v_pk_mul_f32 v[168:169], v[170:171], v[168:169]
	s_nop 0
	v_cvt_pk_bf16_f32 v165, v168, v169
	buffer_store_dwordx4 v[162:165], v155, s[40:43], 0 offen sc1
	v_add_f32_e32 v155, v106, v142
	s_nop 0
	v_min_f32_e32 v162, 0x40e00000, v155
	v_mul_f32_e32 v155, 0xbfd9db23, v162
	v_mul_f32_e32 v155, 0x3fb8aa3b, v155
	v_exp_f32_e32 v155, v155
	v_med3_f32 v164, v161, s13, v222
	v_add_f32_e32 v161, v75, v147
	v_med3_f32 v165, v161, s13, v222
	v_add_f32_e32 v155, 1.0, v155
	v_rcp_f32_e32 v166, v155
	v_add_f32_e32 v155, v107, v143
	v_min_f32_e32 v163, 0x40e00000, v155
	v_mul_f32_e32 v155, 0xbfd9db23, v163
	v_mul_f32_e32 v155, 0x3fb8aa3b, v155
	v_exp_f32_e32 v155, v155
	v_pk_add_f32 v[164:165], v[164:165], 1.0 op_sel_hi:[1,0]
	v_add_f32_e32 v161, v76, v148
	v_add_f32_e32 v155, 1.0, v155
	v_rcp_f32_e32 v167, v155
	v_add_f32_e32 v155, v108, v144
	v_pk_mul_f32 v[162:163], v[162:163], v[166:167]
	s_nop 0
	v_pk_mul_f32 v[162:163], v[164:165], v[162:163]
	v_min_f32_e32 v164, 0x40e00000, v155
	v_mul_f32_e32 v155, 0xbfd9db23, v164
	v_mul_f32_e32 v155, 0x3fb8aa3b, v155
	v_exp_f32_e32 v155, v155
	v_med3_f32 v166, v161, s13, v222
	v_add_f32_e32 v161, v77, v149
	v_med3_f32 v167, v161, s13, v222
	v_add_f32_e32 v155, 1.0, v155
	v_rcp_f32_e32 v168, v155
	v_add_f32_e32 v155, v109, v145
	v_min_f32_e32 v165, 0x40e00000, v155
	v_mul_f32_e32 v155, 0xbfd9db23, v165
	v_mul_f32_e32 v155, 0x3fb8aa3b, v155
	v_exp_f32_e32 v155, v155
	v_pk_add_f32 v[166:167], v[166:167], 1.0 op_sel_hi:[1,0]
	v_add_f32_e32 v161, v70, v138
	v_cvt_pk_bf16_f32 v162, v162, v163
	v_add_f32_e32 v155, 1.0, v155
	v_rcp_f32_e32 v169, v155
	v_add_f32_e32 v155, v102, v134
	v_pk_mul_f32 v[164:165], v[164:165], v[168:169]
	s_nop 0
	v_pk_mul_f32 v[164:165], v[166:167], v[164:165]
	v_min_f32_e32 v166, 0x40e00000, v155
	v_mul_f32_e32 v155, 0xbfd9db23, v166
	v_mul_f32_e32 v155, 0x3fb8aa3b, v155
	v_exp_f32_e32 v155, v155
	v_med3_f32 v168, v161, s13, v222
	v_add_f32_e32 v161, v71, v139
	v_med3_f32 v169, v161, s13, v222
	v_add_f32_e32 v155, 1.0, v155
	v_rcp_f32_e32 v170, v155
	v_add_f32_e32 v155, v103, v135
	v_min_f32_e32 v167, 0x40e00000, v155
	v_mul_f32_e32 v155, 0xbfd9db23, v167
	v_mul_f32_e32 v155, 0x3fb8aa3b, v155
	v_exp_f32_e32 v155, v155
	v_pk_add_f32 v[168:169], v[168:169], 1.0 op_sel_hi:[1,0]
	v_add_f32_e32 v161, v72, v140
	v_cvt_pk_bf16_f32 v163, v164, v165
	v_add_f32_e32 v155, 1.0, v155
	v_rcp_f32_e32 v171, v155
	v_add_f32_e32 v155, v104, v136
	v_pk_mul_f32 v[166:167], v[166:167], v[170:171]
	s_nop 0
	v_pk_mul_f32 v[166:167], v[168:169], v[166:167]
	v_min_f32_e32 v168, 0x40e00000, v155
	v_mul_f32_e32 v155, 0xbfd9db23, v168
	v_mul_f32_e32 v155, 0x3fb8aa3b, v155
	v_exp_f32_e32 v155, v155
	v_med3_f32 v170, v161, s13, v222
	v_add_f32_e32 v161, v73, v141
	v_med3_f32 v171, v161, s13, v222
	v_add_f32_e32 v155, 1.0, v155
	v_rcp_f32_e32 v172, v155
	v_add_f32_e32 v155, v105, v137
	v_min_f32_e32 v169, 0x40e00000, v155
	v_mul_f32_e32 v155, 0xbfd9db23, v169
	v_mul_f32_e32 v155, 0x3fb8aa3b, v155
	v_exp_f32_e32 v155, v155
	v_pk_add_f32 v[170:171], v[170:171], 1.0 op_sel_hi:[1,0]
	v_cvt_pk_bf16_f32 v164, v166, v167
	v_add_f32_e32 v161, v30, v146
	v_add_f32_e32 v155, 1.0, v155
	v_rcp_f32_e32 v173, v155
	v_add_u32_e32 v155, 0x18000, v0
	v_pk_mul_f32 v[168:169], v[168:169], v[172:173]
	s_nop 0
	v_pk_mul_f32 v[168:169], v[170:171], v[168:169]
	s_nop 0
	v_cvt_pk_bf16_f32 v165, v168, v169
	buffer_store_dwordx4 v[162:165], v155, s[40:43], 0 offen sc1
	v_add_f32_e32 v155, v66, v142
	s_nop 0
	v_min_f32_e32 v162, 0x40e00000, v155
	v_mul_f32_e32 v155, 0xbfd9db23, v162
	v_mul_f32_e32 v155, 0x3fb8aa3b, v155
	v_exp_f32_e32 v155, v155
	v_med3_f32 v164, v161, s13, v222
	v_add_f32_e32 v161, v31, v147
	v_med3_f32 v165, v161, s13, v222
	v_add_f32_e32 v155, 1.0, v155
	v_rcp_f32_e32 v166, v155
	v_add_f32_e32 v155, v67, v143
	v_min_f32_e32 v163, 0x40e00000, v155
	v_mul_f32_e32 v155, 0xbfd9db23, v163
	v_mul_f32_e32 v155, 0x3fb8aa3b, v155
	v_exp_f32_e32 v155, v155
	v_pk_add_f32 v[164:165], v[164:165], 1.0 op_sel_hi:[1,0]
	v_add_f32_e32 v161, v32, v148
	v_add_f32_e32 v155, 1.0, v155
	v_rcp_f32_e32 v167, v155
	v_add_f32_e32 v155, v68, v144
	v_pk_mul_f32 v[162:163], v[162:163], v[166:167]
	s_nop 0
	v_pk_mul_f32 v[162:163], v[164:165], v[162:163]
	v_min_f32_e32 v164, 0x40e00000, v155
	v_mul_f32_e32 v155, 0xbfd9db23, v164
	v_mul_f32_e32 v155, 0x3fb8aa3b, v155
	v_exp_f32_e32 v155, v155
	v_med3_f32 v166, v161, s13, v222
	v_add_f32_e32 v161, v33, v149
	v_med3_f32 v167, v161, s13, v222
	v_add_f32_e32 v155, 1.0, v155
	v_rcp_f32_e32 v168, v155
	v_add_f32_e32 v155, v69, v145
	v_min_f32_e32 v165, 0x40e00000, v155
	v_mul_f32_e32 v155, 0xbfd9db23, v165
	v_mul_f32_e32 v155, 0x3fb8aa3b, v155
	v_exp_f32_e32 v155, v155
	v_pk_add_f32 v[166:167], v[166:167], 1.0 op_sel_hi:[1,0]
	v_add_f32_e32 v161, v26, v138
	v_cvt_pk_bf16_f32 v162, v162, v163
	v_add_f32_e32 v155, 1.0, v155
	v_rcp_f32_e32 v169, v155
	v_add_f32_e32 v155, v62, v134
	v_pk_mul_f32 v[164:165], v[164:165], v[168:169]
	s_nop 0
	v_pk_mul_f32 v[164:165], v[166:167], v[164:165]
	v_min_f32_e32 v166, 0x40e00000, v155
	v_mul_f32_e32 v155, 0xbfd9db23, v166
	v_mul_f32_e32 v155, 0x3fb8aa3b, v155
	v_exp_f32_e32 v155, v155
	v_med3_f32 v168, v161, s13, v222
	v_add_f32_e32 v161, v27, v139
	v_med3_f32 v169, v161, s13, v222
	v_add_f32_e32 v155, 1.0, v155
	v_rcp_f32_e32 v170, v155
	v_add_f32_e32 v155, v63, v135
	v_min_f32_e32 v167, 0x40e00000, v155
	v_mul_f32_e32 v155, 0xbfd9db23, v167
	v_mul_f32_e32 v155, 0x3fb8aa3b, v155
	v_exp_f32_e32 v155, v155
	v_pk_add_f32 v[168:169], v[168:169], 1.0 op_sel_hi:[1,0]
	v_add_f32_e32 v161, v28, v140
	v_cvt_pk_bf16_f32 v163, v164, v165
	v_add_f32_e32 v155, 1.0, v155
	v_rcp_f32_e32 v171, v155
	v_add_f32_e32 v155, v64, v136
	v_pk_mul_f32 v[166:167], v[166:167], v[170:171]
	s_nop 0
	v_pk_mul_f32 v[166:167], v[168:169], v[166:167]
	v_min_f32_e32 v168, 0x40e00000, v155
	v_mul_f32_e32 v155, 0xbfd9db23, v168
	v_mul_f32_e32 v155, 0x3fb8aa3b, v155
	v_exp_f32_e32 v155, v155
	v_med3_f32 v170, v161, s13, v222
	v_add_f32_e32 v161, v29, v141
	v_med3_f32 v171, v161, s13, v222
	v_add_f32_e32 v155, 1.0, v155
	v_rcp_f32_e32 v172, v155
	v_add_f32_e32 v155, v65, v137
	v_min_f32_e32 v169, 0x40e00000, v155
	v_mul_f32_e32 v155, 0xbfd9db23, v169
	v_mul_f32_e32 v155, 0x3fb8aa3b, v155
	v_exp_f32_e32 v155, v155
	v_pk_add_f32 v[170:171], v[170:171], 1.0 op_sel_hi:[1,0]
	v_cvt_pk_bf16_f32 v164, v166, v167
	v_add_f32_e32 v161, v22, v146
	v_add_f32_e32 v155, 1.0, v155
	v_rcp_f32_e32 v173, v155
	v_add_u32_e32 v155, 0x40000, v0
	v_pk_mul_f32 v[168:169], v[168:169], v[172:173]
	s_nop 0
	v_pk_mul_f32 v[168:169], v[170:171], v[168:169]
	s_nop 0
	v_cvt_pk_bf16_f32 v165, v168, v169
	buffer_store_dwordx4 v[162:165], v155, s[40:43], 0 offen sc1
	v_add_f32_e32 v155, v58, v142
	s_nop 0
	v_min_f32_e32 v162, 0x40e00000, v155
	v_mul_f32_e32 v155, 0xbfd9db23, v162
	v_mul_f32_e32 v155, 0x3fb8aa3b, v155
	v_exp_f32_e32 v155, v155
	v_med3_f32 v164, v161, s13, v222
	v_add_f32_e32 v161, v23, v147
	v_med3_f32 v165, v161, s13, v222
	v_add_f32_e32 v155, 1.0, v155
	v_rcp_f32_e32 v166, v155
	v_add_f32_e32 v155, v59, v143
	v_min_f32_e32 v163, 0x40e00000, v155
	v_mul_f32_e32 v155, 0xbfd9db23, v163
	v_mul_f32_e32 v155, 0x3fb8aa3b, v155
	v_exp_f32_e32 v155, v155
	v_pk_add_f32 v[164:165], v[164:165], 1.0 op_sel_hi:[1,0]
	v_add_f32_e32 v161, v24, v148
	v_add_f32_e32 v155, 1.0, v155
	v_rcp_f32_e32 v167, v155
	v_add_f32_e32 v155, v60, v144
	v_pk_mul_f32 v[162:163], v[162:163], v[166:167]
	s_nop 0
	v_pk_mul_f32 v[162:163], v[164:165], v[162:163]
	v_min_f32_e32 v164, 0x40e00000, v155
	v_mul_f32_e32 v155, 0xbfd9db23, v164
	v_mul_f32_e32 v155, 0x3fb8aa3b, v155
	v_exp_f32_e32 v155, v155
	v_med3_f32 v166, v161, s13, v222
	v_add_f32_e32 v161, v25, v149
	v_med3_f32 v167, v161, s13, v222
	v_add_f32_e32 v155, 1.0, v155
	v_rcp_f32_e32 v168, v155
	v_add_f32_e32 v155, v61, v145
	v_min_f32_e32 v165, 0x40e00000, v155
	v_mul_f32_e32 v155, 0xbfd9db23, v165
	v_mul_f32_e32 v155, 0x3fb8aa3b, v155
	v_exp_f32_e32 v155, v155
	v_pk_add_f32 v[166:167], v[166:167], 1.0 op_sel_hi:[1,0]
	v_add_f32_e32 v161, v18, v138
	v_cvt_pk_bf16_f32 v162, v162, v163
	v_add_f32_e32 v155, 1.0, v155
	v_rcp_f32_e32 v169, v155
	v_add_f32_e32 v155, v54, v134
	v_pk_mul_f32 v[164:165], v[164:165], v[168:169]
	s_nop 0
	v_pk_mul_f32 v[164:165], v[166:167], v[164:165]
	v_min_f32_e32 v166, 0x40e00000, v155
	v_mul_f32_e32 v155, 0xbfd9db23, v166
	v_mul_f32_e32 v155, 0x3fb8aa3b, v155
	v_exp_f32_e32 v155, v155
	v_med3_f32 v168, v161, s13, v222
	v_add_f32_e32 v161, v19, v139
	v_med3_f32 v169, v161, s13, v222
	v_add_f32_e32 v155, 1.0, v155
	v_rcp_f32_e32 v170, v155
	v_add_f32_e32 v155, v55, v135
	v_min_f32_e32 v167, 0x40e00000, v155
	v_mul_f32_e32 v155, 0xbfd9db23, v167
	v_mul_f32_e32 v155, 0x3fb8aa3b, v155
	v_exp_f32_e32 v155, v155
	v_pk_add_f32 v[168:169], v[168:169], 1.0 op_sel_hi:[1,0]
	v_add_f32_e32 v161, v20, v140
	v_cvt_pk_bf16_f32 v163, v164, v165
	v_add_f32_e32 v155, 1.0, v155
	v_rcp_f32_e32 v171, v155
	v_add_f32_e32 v155, v56, v136
	v_pk_mul_f32 v[166:167], v[166:167], v[170:171]
	s_nop 0
	v_pk_mul_f32 v[166:167], v[168:169], v[166:167]
	v_min_f32_e32 v168, 0x40e00000, v155
	v_mul_f32_e32 v155, 0xbfd9db23, v168
	v_mul_f32_e32 v155, 0x3fb8aa3b, v155
	v_exp_f32_e32 v155, v155
	v_med3_f32 v170, v161, s13, v222
	v_add_f32_e32 v161, v21, v141
	v_med3_f32 v171, v161, s13, v222
	v_add_f32_e32 v155, 1.0, v155
	v_rcp_f32_e32 v172, v155
	v_add_f32_e32 v155, v57, v137
	v_min_f32_e32 v169, 0x40e00000, v155
	v_mul_f32_e32 v155, 0xbfd9db23, v169
	v_mul_f32_e32 v155, 0x3fb8aa3b, v155
	v_exp_f32_e32 v155, v155
	v_pk_add_f32 v[170:171], v[170:171], 1.0 op_sel_hi:[1,0]
	v_cvt_pk_bf16_f32 v164, v166, v167
	v_add_f32_e32 v161, v14, v146
	v_add_f32_e32 v155, 1.0, v155
	v_rcp_f32_e32 v173, v155
	v_add_u32_e32 v155, 0x48000, v0
	v_add_f32_e32 v146, v6, v146
	v_med3_f32 v146, v146, s13, v222
	v_pk_mul_f32 v[168:169], v[168:169], v[172:173]
	s_nop 0
	v_pk_mul_f32 v[168:169], v[170:171], v[168:169]
	s_nop 0
	v_cvt_pk_bf16_f32 v165, v168, v169
	buffer_store_dwordx4 v[162:165], v155, s[40:43], 0 offen sc1
	v_add_f32_e32 v155, v50, v142
	v_add_f32_e32 v142, v42, v142
	v_min_f32_e32 v162, 0x40e00000, v155
	v_mul_f32_e32 v155, 0xbfd9db23, v162
	v_mul_f32_e32 v155, 0x3fb8aa3b, v155
	v_exp_f32_e32 v155, v155
	v_med3_f32 v164, v161, s13, v222
	v_add_f32_e32 v161, v15, v147
	v_med3_f32 v165, v161, s13, v222
	v_add_f32_e32 v155, 1.0, v155
	v_rcp_f32_e32 v166, v155
	v_add_f32_e32 v155, v51, v143
	v_min_f32_e32 v163, 0x40e00000, v155
	v_mul_f32_e32 v155, 0xbfd9db23, v163
	v_mul_f32_e32 v155, 0x3fb8aa3b, v155
	v_exp_f32_e32 v155, v155
	v_pk_add_f32 v[164:165], v[164:165], 1.0 op_sel_hi:[1,0]
	v_add_f32_e32 v161, v16, v148
	v_min_f32_e32 v142, 0x40e00000, v142
	v_add_f32_e32 v155, 1.0, v155
	v_rcp_f32_e32 v167, v155
	v_add_f32_e32 v155, v52, v144
	v_add_f32_e32 v143, v43, v143
	v_min_f32_e32 v143, 0x40e00000, v143
	v_pk_mul_f32 v[162:163], v[162:163], v[166:167]
	v_med3_f32 v166, v161, s13, v222
	v_pk_mul_f32 v[162:163], v[164:165], v[162:163]
	v_min_f32_e32 v164, 0x40e00000, v155
	v_mul_f32_e32 v155, 0xbfd9db23, v164
	v_mul_f32_e32 v155, 0x3fb8aa3b, v155
	v_exp_f32_e32 v155, v155
	v_add_f32_e32 v161, v17, v149
	v_med3_f32 v167, v161, s13, v222
	v_pk_add_f32 v[166:167], v[166:167], 1.0 op_sel_hi:[1,0]
	v_add_f32_e32 v155, 1.0, v155
	v_rcp_f32_e32 v168, v155
	v_add_f32_e32 v155, v53, v145
	v_min_f32_e32 v165, 0x40e00000, v155
	v_mul_f32_e32 v155, 0xbfd9db23, v165
	v_mul_f32_e32 v155, 0x3fb8aa3b, v155
	v_exp_f32_e32 v155, v155
	v_add_f32_e32 v161, v10, v138
	v_cvt_pk_bf16_f32 v162, v162, v163
	v_add_f32_e32 v147, v7, v147
	v_add_f32_e32 v155, 1.0, v155
	v_rcp_f32_e32 v169, v155
	v_add_f32_e32 v155, v46, v134
	v_med3_f32 v147, v147, s13, v222
	v_add_f32_e32 v144, v44, v144
	v_pk_mul_f32 v[164:165], v[164:165], v[168:169]
	v_med3_f32 v168, v161, s13, v222
	v_pk_mul_f32 v[164:165], v[166:167], v[164:165]
	v_min_f32_e32 v166, 0x40e00000, v155
	v_mul_f32_e32 v155, 0xbfd9db23, v166
	v_mul_f32_e32 v155, 0x3fb8aa3b, v155
	v_exp_f32_e32 v155, v155
	v_add_f32_e32 v161, v11, v139
	v_med3_f32 v169, v161, s13, v222
	v_pk_add_f32 v[168:169], v[168:169], 1.0 op_sel_hi:[1,0]
	v_add_f32_e32 v155, 1.0, v155
	v_rcp_f32_e32 v170, v155
	v_add_f32_e32 v155, v47, v135
	v_min_f32_e32 v167, 0x40e00000, v155
	v_mul_f32_e32 v155, 0xbfd9db23, v167
	v_mul_f32_e32 v155, 0x3fb8aa3b, v155
	v_exp_f32_e32 v155, v155
	v_add_f32_e32 v161, v12, v140
	v_cvt_pk_bf16_f32 v163, v164, v165
	v_pk_add_f32 v[146:147], v[146:147], 1.0 op_sel_hi:[1,0]
	v_add_f32_e32 v155, 1.0, v155
	v_rcp_f32_e32 v171, v155
	v_add_f32_e32 v155, v48, v136
	v_min_f32_e32 v144, 0x40e00000, v144
	v_add_f32_e32 v145, v45, v145
	v_pk_mul_f32 v[166:167], v[166:167], v[170:171]
	v_med3_f32 v170, v161, s13, v222
	v_pk_mul_f32 v[166:167], v[168:169], v[166:167]
	v_min_f32_e32 v168, 0x40e00000, v155
	v_mul_f32_e32 v155, 0xbfd9db23, v168
	v_mul_f32_e32 v155, 0x3fb8aa3b, v155
	v_exp_f32_e32 v155, v155
	v_add_f32_e32 v161, v13, v141
	v_med3_f32 v171, v161, s13, v222
	v_pk_add_f32 v[170:171], v[170:171], 1.0 op_sel_hi:[1,0]
	v_add_f32_e32 v155, 1.0, v155
	v_rcp_f32_e32 v172, v155
	v_add_f32_e32 v155, v49, v137
	v_min_f32_e32 v169, 0x40e00000, v155
	v_mul_f32_e32 v155, 0xbfd9db23, v169
	v_mul_f32_e32 v155, 0x3fb8aa3b, v155
	v_exp_f32_e32 v155, v155
	v_cvt_pk_bf16_f32 v164, v166, v167
	v_min_f32_e32 v145, 0x40e00000, v145
	v_add_f32_e32 v134, v38, v134
	v_add_f32_e32 v155, 1.0, v155
	v_rcp_f32_e32 v173, v155
	v_add_u32_e32 v155, 0x50000, v0
	v_add_f32_e32 v135, v39, v135
	v_min_f32_e32 v134, 0x40e00000, v134
	v_pk_mul_f32 v[168:169], v[168:169], v[172:173]
	v_min_f32_e32 v135, 0x40e00000, v135
	v_pk_mul_f32 v[168:169], v[170:171], v[168:169]
	v_add_f32_e32 v138, v2, v138
	v_cvt_pk_bf16_f32 v165, v168, v169
	buffer_store_dwordx4 v[162:165], v155, s[40:43], 0 offen sc1
	v_mul_f32_e32 v155, 0xbfd9db23, v142
	v_mul_f32_e32 v155, 0x3fb8aa3b, v155
	v_exp_f32_e32 v155, v155
	v_add_f32_e32 v139, v3, v139
	v_med3_f32 v138, v138, s13, v222
	v_med3_f32 v139, v139, s13, v222
	v_add_f32_e32 v155, 1.0, v155
	v_rcp_f32_e32 v162, v155
	v_mul_f32_e32 v155, 0xbfd9db23, v143
	v_mul_f32_e32 v155, 0x3fb8aa3b, v155
	v_exp_f32_e32 v155, v155
	v_pk_add_f32 v[138:139], v[138:139], 1.0 op_sel_hi:[1,0]
	v_add_u32_e32 v0, 0x58000, v0
	v_add_f32_e32 v155, 1.0, v155
	v_rcp_f32_e32 v163, v155
	s_nop 0
	v_pk_mul_f32 v[142:143], v[142:143], v[162:163]
	s_nop 0
	v_pk_mul_f32 v[142:143], v[146:147], v[142:143]
	v_mul_f32_e32 v147, 0xbfd9db23, v144
	v_mul_f32_e32 v147, 0x3fb8aa3b, v147
	v_exp_f32_e32 v147, v147
	v_add_f32_e32 v146, v8, v148
	v_med3_f32 v146, v146, s13, v222
	v_add_f32_e32 v147, 1.0, v147
	v_rcp_f32_e32 v148, v147
	v_add_f32_e32 v147, v9, v149
	v_mul_f32_e32 v149, 0xbfd9db23, v145
	v_mul_f32_e32 v149, 0x3fb8aa3b, v149
	v_exp_f32_e32 v149, v149
	v_med3_f32 v147, v147, s13, v222
	v_pk_add_f32 v[146:147], v[146:147], 1.0 op_sel_hi:[1,0]
	v_add_f32_e32 v149, 1.0, v149
	v_rcp_f32_e32 v149, v149
	s_nop 0
	v_pk_mul_f32 v[144:145], v[144:145], v[148:149]
	s_nop 0
	v_pk_mul_f32 v[144:145], v[146:147], v[144:145]
	v_mul_f32_e32 v146, 0xbfd9db23, v134
	v_mul_f32_e32 v147, 0xbfd9db23, v135
	v_mul_f32_e32 v146, 0x3fb8aa3b, v146
	v_mul_f32_e32 v147, 0x3fb8aa3b, v147
	v_exp_f32_e32 v146, v146
	v_exp_f32_e32 v147, v147
	v_add_f32_e32 v146, 1.0, v146
	v_add_f32_e32 v147, 1.0, v147
	v_rcp_f32_e32 v146, v146
	v_rcp_f32_e32 v147, v147
	s_nop 0
	v_pk_mul_f32 v[134:135], v[134:135], v[146:147]
	s_nop 0
	v_pk_mul_f32 v[138:139], v[138:139], v[134:135]
	v_add_f32_e32 v134, v40, v136
	v_add_f32_e32 v135, v4, v140
	v_min_f32_e32 v134, 0x40e00000, v134
	v_med3_f32 v136, v135, s13, v222
	v_mul_f32_e32 v135, 0xbfd9db23, v134
	v_mul_f32_e32 v135, 0x3fb8aa3b, v135
	v_exp_f32_e32 v135, v135
	s_nop 0
	v_add_f32_e32 v135, 1.0, v135
	v_rcp_f32_e32 v140, v135
	v_add_f32_e32 v135, v41, v137
	v_min_f32_e32 v135, 0x40e00000, v135
	v_add_f32_e32 v137, v5, v141
	v_mul_f32_e32 v141, 0xbfd9db23, v135
	v_mul_f32_e32 v141, 0x3fb8aa3b, v141
	v_exp_f32_e32 v141, v141
	v_med3_f32 v137, v137, s13, v222
	v_pk_add_f32 v[136:137], v[136:137], 1.0 op_sel_hi:[1,0]
	v_add_f32_e32 v141, 1.0, v141
	v_rcp_f32_e32 v141, v141
	s_nop 0
	v_pk_mul_f32 v[134:135], v[134:135], v[140:141]
	s_nop 0
	v_pk_mul_f32 v[140:141], v[136:137], v[134:135]
	v_cvt_pk_bf16_f32 v134, v142, v143
	v_cvt_pk_bf16_f32 v135, v144, v145
	v_cvt_pk_bf16_f32 v136, v138, v139
	v_cvt_pk_bf16_f32 v137, v140, v141
	buffer_store_dwordx4 v[134:137], v0, s[40:43], 0 offen sc1
	s_waitcnt vmcnt(8)
	s_add_u32 s42, s29, 0xffffff00
	s_addc_u32 s43, s31, -1
	s_and_b64 vcc, exec, s[0:1]
	s_cbranch_vccz .LBB0_2070
